# v60 + stacked neutral edits: P2 spatial load ladders de-serialised, satisfied lgkmcnt waits / mid setprio pairs / m0 save-restore removed, compiler vmcnt(0) at P5-P6 unit heads removed
# baseline (speedup 1.0000x reference)
; #define LAS __attribute__((address_space(3)))
; #define PG8_STAGEA(bufoff, gbase, h) PG8_STAGE2(bufoff, gbase, voffA[h][0], voffA[h][1])
; #define PG8_LDA(dst, b, h) do { _Pragma("unroll") for (int m = 0; m < 4; ++m) _Pragma("unroll") for (int k = 0; k < 2; ++k) dst[m][k] = *(const LAS bf16x8*)(lds + PG8_SA(b, h) + aoff + m * 2048 + k * 1024); } while (0)
; #define PG8_LDB(dst, b, h) do { _Pragma("unroll") for (int n = 0; n < 2; ++n) _Pragma("unroll") for (int k = 0; k < 2; ++k) dst[n][k] = *(const LAS bf16x8*)(lds + PG8_SB(b, h) + boff + n * 2048 + k * 1024); } while (0)
; #define PG8_WAIT_K0() do { if (EST > 0 && t == 0 && ui > 0) asm volatile("s_waitcnt vmcnt(%0)" :: "n"((HM ? 6 : 8) + EST) : "memory"); else PG8_WAIT_K(); } while (0)
; #define PG8_WAIT_L(n) asm volatile("s_waitcnt lgkmcnt(" #n ")" ::: "memory")
; #define PG8_BAR __builtin_amdgcn_s_barrier()
; #define PG8_SCHED __builtin_amdgcn_sched_barrier(0)
;     ...
;             PG8_LDB(B0, 0, 0); PG8_LDB(B1, 0, 1); PG8_SCHED; PG8_LDA(At, 0, 0); if constexpr (!HM) PG8_STAGEA(PG8_SA(1, 1), a1, 1);
;             if constexpr (Sched::kGather) { if (last && has_next) { const u32x4 tn = *(const LAS u32x4*)(S.aux + tid * 16); voffA[0][0] = tn.x; voffA[0][1] = tn.y; voffA[1][0] = tn.z; voffA[1][1] = tn.w; } }
;             PG8_WAIT_K0(); PG8_WAIT_L(0); PG8_BAR; PG8_MMA(0, 0, At, B0); PG8_MMA(0, 1, At, B1); PG8_BAR; PG8_SCHED;
.LBB0_574:
	ds_read_b128 v[18:21], v167
	ds_read_b128 v[22:25], v167 offset:1024
	ds_read_b128 v[26:29], v167 offset:2048
	ds_read_b128 v[30:33], v167 offset:3072
	ds_read_b128 v[2:5], v168
	ds_read_b128 v[6:9], v168 offset:1024
	ds_read_b128 v[10:13], v168 offset:2048
	ds_read_b128 v[14:17], v168 offset:3072
	s_cmp_lg_u32 s42, 0
	s_cselect_b64 s[42:43], -1, 0
	s_add_u32 s44, s38, 0x80
	s_addc_u32 s45, s39, 0
	ds_read_b128 v[74:77], v169
	ds_read_b128 v[78:81], v169 offset:1024
	ds_read_b128 v[82:85], v169 offset:2048
	ds_read_b128 v[90:93], v169 offset:3072
	ds_read_b128 v[94:97], v169 offset:4096
	ds_read_b128 v[98:101], v169 offset:5120
	ds_read_b128 v[70:73], v169 offset:6144
	ds_read_b128 v[86:89], v169 offset:7168
	s_mov_b32 m0, s68
	s_nop 0
	global_load_lds_dwordx4 v162, s[44:45]
	s_and_b64 vcc, exec, s[42:43]
	s_mov_b32 m0, s69
	s_nop 0
	global_load_lds_dwordx4 v163, s[44:45]
	s_cbranch_vccz .LBB0_587
	s_waitcnt vmcnt(24)
	s_cbranch_execnz .LBB0_577

; #define LAS __attribute__((address_space(3)))
; #define PG8_STAGEA(bufoff, gbase, h) PG8_STAGE2(bufoff, gbase, voffA[h][0], voffA[h][1])
; #define PG8_LDA(dst, b, h) do { _Pragma("unroll") for (int m = 0; m < 4; ++m) _Pragma("unroll") for (int k = 0; k < 2; ++k) dst[m][k] = *(const LAS bf16x8*)(lds + PG8_SA(b, h) + aoff + m * 2048 + k * 1024); } while (0)
; #define PG8_LDB(dst, b, h) do { _Pragma("unroll") for (int n = 0; n < 2; ++n) _Pragma("unroll") for (int k = 0; k < 2; ++k) dst[n][k] = *(const LAS bf16x8*)(lds + PG8_SB(b, h) + boff + n * 2048 + k * 1024); } while (0)
; #define PG8_WAIT_K0() do { if (EST > 0 && t == 0 && ui > 0) asm volatile("s_waitcnt vmcnt(%0)" :: "n"((HM ? 6 : 8) + EST) : "memory"); else PG8_WAIT_K(); } while (0)
; #define PG8_WAIT_L(n) asm volatile("s_waitcnt lgkmcnt(" #n ")" ::: "memory")
; #define PG8_BAR __builtin_amdgcn_s_barrier()
; #define PG8_SCHED __builtin_amdgcn_sched_barrier(0)
;     ...
;             PG8_LDB(B0, 0, 0); PG8_LDB(B1, 0, 1); PG8_SCHED; PG8_LDA(At, 0, 0); if constexpr (!HM) PG8_STAGEA(PG8_SA(1, 1), a1, 1);
;             if constexpr (Sched::kGather) { if (last && has_next) { const u32x4 tn = *(const LAS u32x4*)(S.aux + tid * 16); voffA[0][0] = tn.x; voffA[0][1] = tn.y; voffA[1][0] = tn.z; voffA[1][1] = tn.w; } }
;             PG8_WAIT_K0(); PG8_WAIT_L(0); PG8_BAR; PG8_MMA(0, 0, At, B0); PG8_MMA(0, 1, At, B1); PG8_BAR; PG8_SCHED;
.LBB0_604:
	ds_read_b128 v[18:21], v180
	ds_read_b128 v[22:25], v180 offset:1024
	ds_read_b128 v[26:29], v180 offset:2048
	ds_read_b128 v[30:33], v180 offset:3072
	ds_read_b128 v[2:5], v181
	ds_read_b128 v[6:9], v181 offset:1024
	ds_read_b128 v[10:13], v181 offset:2048
	ds_read_b128 v[14:17], v181 offset:3072
	s_cmp_lg_u32 s28, 0
	s_cselect_b64 s[28:29], -1, 0
	s_add_u32 s30, s24, 0x80
	s_addc_u32 s31, s25, 0
	ds_read_b128 v[70:73], v182
	ds_read_b128 v[82:85], v182 offset:1024
	ds_read_b128 v[86:89], v182 offset:2048
	ds_read_b128 v[98:101], v182 offset:3072
	ds_read_b128 v[90:93], v182 offset:4096
	ds_read_b128 v[94:97], v182 offset:5120
	ds_read_b128 v[74:77], v182 offset:6144
	ds_read_b128 v[78:81], v182 offset:7168
	s_mov_b32 m0, s53
	s_nop 0
	global_load_lds_dwordx4 v175, s[30:31]
	s_and_b64 vcc, exec, s[28:29]
	s_mov_b32 m0, s54
	s_nop 0
	global_load_lds_dwordx4 v176, s[30:31]
	s_cbranch_vccz .LBB0_617
	s_waitcnt vmcnt(24)
	s_cbranch_execnz .LBB0_607

; #define LAS __attribute__((address_space(3)))
; #define PG8_STAGEA(bufoff, gbase, h) PG8_STAGE2(bufoff, gbase, voffA[h][0], voffA[h][1])
; #define PG8_LDA(dst, b, h) do { _Pragma("unroll") for (int m = 0; m < 4; ++m) _Pragma("unroll") for (int k = 0; k < 2; ++k) dst[m][k] = *(const LAS bf16x8*)(lds + PG8_SA(b, h) + aoff + m * 2048 + k * 1024); } while (0)
; #define PG8_LDB(dst, b, h) do { _Pragma("unroll") for (int n = 0; n < 2; ++n) _Pragma("unroll") for (int k = 0; k < 2; ++k) dst[n][k] = *(const LAS bf16x8*)(lds + PG8_SB(b, h) + boff + n * 2048 + k * 1024); } while (0)
; #define PG8_WAIT_K0() do { if (EST > 0 && t == 0 && ui > 0) asm volatile("s_waitcnt vmcnt(%0)" :: "n"((HM ? 6 : 8) + EST) : "memory"); else PG8_WAIT_K(); } while (0)
; #define PG8_WAIT_L(n) asm volatile("s_waitcnt lgkmcnt(" #n ")" ::: "memory")
; #define PG8_BAR __builtin_amdgcn_s_barrier()
; #define PG8_SCHED __builtin_amdgcn_sched_barrier(0)
;     ...
;             PG8_LDB(B0, 0, 0); PG8_LDB(B1, 0, 1); PG8_SCHED; PG8_LDA(At, 0, 0); if constexpr (!HM) PG8_STAGEA(PG8_SA(1, 1), a1, 1);
;             if constexpr (Sched::kGather) { if (last && has_next) { const u32x4 tn = *(const LAS u32x4*)(S.aux + tid * 16); voffA[0][0] = tn.x; voffA[0][1] = tn.y; voffA[1][0] = tn.z; voffA[1][1] = tn.w; } }
;             PG8_WAIT_K0(); PG8_WAIT_L(0); PG8_BAR; PG8_MMA(0, 0, At, B0); PG8_MMA(0, 1, At, B1); PG8_BAR; PG8_SCHED;
.LBB0_691:
	ds_read_b128 v[18:21], v208
	ds_read_b128 v[22:25], v208 offset:1024
	ds_read_b128 v[26:29], v208 offset:2048
	ds_read_b128 v[30:33], v208 offset:3072
	s_waitcnt lgkmcnt(4)
	ds_read_b128 v[2:5], v209
	ds_read_b128 v[6:9], v209 offset:1024
	ds_read_b128 v[10:13], v209 offset:2048
	ds_read_b128 v[14:17], v209 offset:3072
	s_cmp_lg_u32 s28, 0
	s_cselect_b64 s[28:29], -1, 0
	s_add_u32 s36, s30, 0x80
	s_addc_u32 s37, s31, 0
	ds_read_b128 v[74:77], v210
	ds_read_b128 v[82:85], v210 offset:1024
	ds_read_b128 v[90:93], v210 offset:2048
	ds_read_b128 v[98:101], v210 offset:3072
	ds_read_b128 v[86:89], v210 offset:4096
	ds_read_b128 v[94:97], v210 offset:5120
	ds_read_b128 v[70:73], v210 offset:6144
	ds_read_b128 v[78:81], v210 offset:7168
	s_mov_b32 m0, s58
	s_nop 0
	global_load_lds_dwordx4 v203, s[36:37]
	s_and_b64 vcc, exec, s[28:29]
	s_mov_b32 m0, s59
	s_nop 0
	global_load_lds_dwordx4 v204, s[36:37]
	s_cbranch_vccz .LBB0_720
	s_waitcnt vmcnt(40)
	s_cbranch_execnz .LBB0_694
